# v23 + loop-edge edit: the K-loop counter / pointer / exit-test SALU block moved in front of the loop-back barrier in the four GEMM K-loops
# speedup vs baseline: 1.0056x; 1.0056x over previous
.LBB0_157:
	ds_read_b128 v[150:153], v163
	ds_read_b128 v[154:157], v164
	ds_read_b128 v[178:181], v158
	ds_read_b128 v[182:185], v159
	ds_read_b128 v[186:189], v165
	ds_read_b128 v[190:193], v166
	ds_read_b128 v[194:197], v167
	ds_read_b128 v[198:201], v168
	s_add_u32 s44, s42, 0x80
	s_addc_u32 s45, s43, 0
	s_cmp_eq_u32 s73, 28
	s_cselect_b32 s47, s31, s45
	s_cselect_b32 s46, s39, s44
	s_cselect_b32 s45, s29, s72
	s_cselect_b32 s44, s70, s71
	v_lshl_add_u64 v[234:235], s[42:43], 0, v[142:143]
	s_add_i32 m0, s21, 0xc000
	ds_read_b128 v[202:205], v176
	ds_read_b128 v[206:209], v176 offset:1024
	ds_read_b128 v[210:213], v176 offset:2048
	ds_read_b128 v[214:217], v176 offset:3072
	ds_read_b128 v[218:221], v176 offset:4096
	ds_read_b128 v[222:225], v176 offset:5120
	ds_read_b128 v[226:229], v176 offset:6144
	ds_read_b128 v[230:233], v176 offset:7168
	global_load_lds_dwordx4 v[234:235], off
	v_lshl_add_u64 v[234:235], s[42:43], 0, v[144:145]
	s_add_i32 m0, s21, 0xe000
	s_nop 0
	global_load_lds_dwordx4 v[234:235], off
	s_waitcnt vmcnt(8)
	s_waitcnt lgkmcnt(0)
	s_barrier
	s_setprio 1
	s_waitcnt lgkmcnt(0)
	v_mfma_f32_16x16x32_bf16 v[126:129], v[178:181], v[202:205], v[126:129]
	v_mfma_f32_16x16x32_bf16 v[122:125], v[154:157], v[202:205], v[122:125]
	v_mfma_f32_16x16x32_bf16 v[110:113], v[178:181], v[210:213], v[110:113]
	v_mfma_f32_16x16x32_bf16 v[106:109], v[154:157], v[210:213], v[106:109]
	v_mfma_f32_16x16x32_bf16 v[94:97], v[178:181], v[218:221], v[94:97]
	v_mfma_f32_16x16x32_bf16 v[90:93], v[154:157], v[218:221], v[90:93]
	v_mfma_f32_16x16x32_bf16 v[78:81], v[178:181], v[226:229], v[78:81]
	v_mfma_f32_16x16x32_bf16 v[74:77], v[154:157], v[226:229], v[74:77]
	v_mfma_f32_16x16x32_bf16 v[126:129], v[150:153], v[206:209], v[126:129]
	v_mfma_f32_16x16x32_bf16 v[122:125], v[186:189], v[206:209], v[122:125]
	v_mfma_f32_16x16x32_bf16 v[110:113], v[150:153], v[214:217], v[110:113]
	v_mfma_f32_16x16x32_bf16 v[106:109], v[186:189], v[214:217], v[106:109]
	v_mfma_f32_16x16x32_bf16 v[94:97], v[150:153], v[222:225], v[94:97]
	v_mfma_f32_16x16x32_bf16 v[90:93], v[186:189], v[222:225], v[90:93]
	v_mfma_f32_16x16x32_bf16 v[78:81], v[150:153], v[230:233], v[78:81]
	v_mfma_f32_16x16x32_bf16 v[74:77], v[186:189], v[230:233], v[74:77]
	s_setprio 0
	s_setprio 1
	v_mfma_f32_16x16x32_bf16 v[118:121], v[182:185], v[202:205], v[118:121]
	v_mfma_f32_16x16x32_bf16 v[114:117], v[194:197], v[202:205], v[114:117]
	v_mfma_f32_16x16x32_bf16 v[102:105], v[182:185], v[210:213], v[102:105]
	v_mfma_f32_16x16x32_bf16 v[98:101], v[194:197], v[210:213], v[98:101]
	v_mfma_f32_16x16x32_bf16 v[86:89], v[182:185], v[218:221], v[86:89]
	v_mfma_f32_16x16x32_bf16 v[82:85], v[194:197], v[218:221], v[82:85]
	v_mfma_f32_16x16x32_bf16 v[70:73], v[182:185], v[226:229], v[70:73]
	v_mfma_f32_16x16x32_bf16 v[66:69], v[194:197], v[226:229], v[66:69]
	v_mfma_f32_16x16x32_bf16 v[118:121], v[190:193], v[206:209], v[118:121]
	v_mfma_f32_16x16x32_bf16 v[114:117], v[198:201], v[206:209], v[114:117]
	v_mfma_f32_16x16x32_bf16 v[102:105], v[190:193], v[214:217], v[102:105]
	v_mfma_f32_16x16x32_bf16 v[98:101], v[198:201], v[214:217], v[98:101]
	v_mfma_f32_16x16x32_bf16 v[86:89], v[190:193], v[222:225], v[86:89]
	v_mfma_f32_16x16x32_bf16 v[82:85], v[198:201], v[222:225], v[82:85]
	v_mfma_f32_16x16x32_bf16 v[70:73], v[190:193], v[230:233], v[70:73]
	v_mfma_f32_16x16x32_bf16 v[66:69], v[198:201], v[230:233], v[66:69]
	s_setprio 0
	s_barrier
	s_mov_b32 m0, s23
	v_lshl_add_u64 v[234:235], s[44:45], 0, v[130:131]
	s_add_u32 s74, s44, 0x80000
	ds_read_b128 v[202:205], v176 offset:16384
	ds_read_b128 v[206:209], v176 offset:17408
	ds_read_b128 v[210:213], v176 offset:18432
	ds_read_b128 v[214:217], v176 offset:19456
	ds_read_b128 v[218:221], v176 offset:20480
	ds_read_b128 v[222:225], v176 offset:21504
	ds_read_b128 v[226:229], v176 offset:22528
	ds_read_b128 v[230:233], v176 offset:23552
	global_load_lds_dwordx4 v[234:235], off
	v_lshl_add_u64 v[236:237], s[44:45], 0, v[136:137]
	s_mov_b32 m0, s25
	s_addc_u32 s75, s45, 0
	global_load_lds_dwordx4 v[236:237], off
	v_lshl_add_u64 v[238:239], s[74:75], 0, v[130:131]
	s_mov_b32 m0, s27
	v_lshl_add_u64 v[240:241], s[46:47], 0, v[138:139]
	global_load_lds_dwordx4 v[238:239], off
	v_lshl_add_u64 v[238:239], s[74:75], 0, v[136:137]
	s_mov_b32 m0, s33
	s_nop 0
	global_load_lds_dwordx4 v[238:239], off
	v_lshl_add_u64 v[238:239], s[46:47], 0, v[132:133]
	s_mov_b32 m0, s21
	s_nop 0
	global_load_lds_dwordx4 v[238:239], off
	s_mov_b32 m0, s41
	s_nop 0
	global_load_lds_dwordx4 v[240:241], off
	s_waitcnt vmcnt(8)
	s_waitcnt lgkmcnt(0)
	s_barrier
	s_setprio 1
	s_waitcnt lgkmcnt(0)
	v_mfma_f32_16x16x32_bf16 v[62:65], v[178:181], v[202:205], v[62:65]
	v_mfma_f32_16x16x32_bf16 v[58:61], v[154:157], v[202:205], v[58:61]
	v_mfma_f32_16x16x32_bf16 v[46:49], v[178:181], v[210:213], v[46:49]
	v_mfma_f32_16x16x32_bf16 v[42:45], v[154:157], v[210:213], v[42:45]
	v_mfma_f32_16x16x32_bf16 v[30:33], v[178:181], v[218:221], v[30:33]
	v_mfma_f32_16x16x32_bf16 v[26:29], v[154:157], v[218:221], v[26:29]
	v_mfma_f32_16x16x32_bf16 v[14:17], v[178:181], v[226:229], v[14:17]
	v_mfma_f32_16x16x32_bf16 v[10:13], v[154:157], v[226:229], v[10:13]
	v_mfma_f32_16x16x32_bf16 v[62:65], v[150:153], v[206:209], v[62:65]
	v_mfma_f32_16x16x32_bf16 v[58:61], v[186:189], v[206:209], v[58:61]
	v_mfma_f32_16x16x32_bf16 v[46:49], v[150:153], v[214:217], v[46:49]
	v_mfma_f32_16x16x32_bf16 v[42:45], v[186:189], v[214:217], v[42:45]
	v_mfma_f32_16x16x32_bf16 v[30:33], v[150:153], v[222:225], v[30:33]
	v_mfma_f32_16x16x32_bf16 v[26:29], v[186:189], v[222:225], v[26:29]
	v_mfma_f32_16x16x32_bf16 v[14:17], v[150:153], v[230:233], v[14:17]
	v_mfma_f32_16x16x32_bf16 v[10:13], v[186:189], v[230:233], v[10:13]
	s_setprio 0
	s_setprio 1
	v_mfma_f32_16x16x32_bf16 v[54:57], v[182:185], v[202:205], v[54:57]
	v_mfma_f32_16x16x32_bf16 v[50:53], v[194:197], v[202:205], v[50:53]
	v_mfma_f32_16x16x32_bf16 v[38:41], v[182:185], v[210:213], v[38:41]
	v_mfma_f32_16x16x32_bf16 v[34:37], v[194:197], v[210:213], v[34:37]
	v_mfma_f32_16x16x32_bf16 v[18:21], v[182:185], v[218:221], v[18:21]
	v_mfma_f32_16x16x32_bf16 v[22:25], v[194:197], v[218:221], v[22:25]
	v_mfma_f32_16x16x32_bf16 v[2:5], v[182:185], v[226:229], v[2:5]
	v_mfma_f32_16x16x32_bf16 v[6:9], v[194:197], v[226:229], v[6:9]
	v_mfma_f32_16x16x32_bf16 v[54:57], v[190:193], v[206:209], v[54:57]
	v_mfma_f32_16x16x32_bf16 v[50:53], v[198:201], v[206:209], v[50:53]
	v_mfma_f32_16x16x32_bf16 v[38:41], v[190:193], v[214:217], v[38:41]
	v_mfma_f32_16x16x32_bf16 v[34:37], v[198:201], v[214:217], v[34:37]
	v_mfma_f32_16x16x32_bf16 v[18:21], v[190:193], v[222:225], v[18:21]
	v_mfma_f32_16x16x32_bf16 v[22:25], v[198:201], v[222:225], v[22:25]
	v_mfma_f32_16x16x32_bf16 v[2:5], v[190:193], v[230:233], v[2:5]
	v_mfma_f32_16x16x32_bf16 v[6:9], v[198:201], v[230:233], v[6:9]
	s_setprio 0
	s_barrier
	ds_read_b128 v[150:153], v169
	ds_read_b128 v[154:157], v170
	ds_read_b128 v[178:181], v160
	ds_read_b128 v[182:185], v161
	ds_read_b128 v[186:189], v171
	ds_read_b128 v[190:193], v172
	ds_read_b128 v[194:197], v173
	ds_read_b128 v[198:201], v174
	s_mov_b32 m0, s53
	v_lshl_add_u64 v[242:243], s[46:47], 0, v[134:135]
	ds_read_b128 v[202:205], v176 offset:32768
	ds_read_b128 v[206:209], v176 offset:33792
	ds_read_b128 v[210:213], v176 offset:34816
	ds_read_b128 v[214:217], v176 offset:35840
	ds_read_b128 v[218:221], v176 offset:36864
	ds_read_b128 v[222:225], v176 offset:37888
	ds_read_b128 v[226:229], v176 offset:38912
	ds_read_b128 v[230:233], v176 offset:39936
	global_load_lds_dwordx4 v[242:243], off
	v_lshl_add_u64 v[242:243], s[46:47], 0, v[140:141]
	s_mov_b32 m0, s55
	s_nop 0
	global_load_lds_dwordx4 v[242:243], off
	s_waitcnt vmcnt(8)
	s_waitcnt lgkmcnt(0)
	s_barrier
	s_setprio 1
	s_waitcnt lgkmcnt(0)
	v_mfma_f32_16x16x32_bf16 v[126:129], v[178:181], v[202:205], v[126:129]
	v_mfma_f32_16x16x32_bf16 v[122:125], v[154:157], v[202:205], v[122:125]
	v_mfma_f32_16x16x32_bf16 v[110:113], v[178:181], v[210:213], v[110:113]
	v_mfma_f32_16x16x32_bf16 v[106:109], v[154:157], v[210:213], v[106:109]
	v_mfma_f32_16x16x32_bf16 v[94:97], v[178:181], v[218:221], v[94:97]
	v_mfma_f32_16x16x32_bf16 v[90:93], v[154:157], v[218:221], v[90:93]
	v_mfma_f32_16x16x32_bf16 v[78:81], v[178:181], v[226:229], v[78:81]
	v_mfma_f32_16x16x32_bf16 v[74:77], v[154:157], v[226:229], v[74:77]
	v_mfma_f32_16x16x32_bf16 v[126:129], v[150:153], v[206:209], v[126:129]
	v_mfma_f32_16x16x32_bf16 v[122:125], v[186:189], v[206:209], v[122:125]
	v_mfma_f32_16x16x32_bf16 v[110:113], v[150:153], v[214:217], v[110:113]
	v_mfma_f32_16x16x32_bf16 v[106:109], v[186:189], v[214:217], v[106:109]
	v_mfma_f32_16x16x32_bf16 v[94:97], v[150:153], v[222:225], v[94:97]
	v_mfma_f32_16x16x32_bf16 v[90:93], v[186:189], v[222:225], v[90:93]
	v_mfma_f32_16x16x32_bf16 v[78:81], v[150:153], v[230:233], v[78:81]
	v_mfma_f32_16x16x32_bf16 v[74:77], v[186:189], v[230:233], v[74:77]
	s_setprio 0
	s_setprio 1
	v_mfma_f32_16x16x32_bf16 v[118:121], v[182:185], v[202:205], v[118:121]
	v_mfma_f32_16x16x32_bf16 v[114:117], v[194:197], v[202:205], v[114:117]
	v_mfma_f32_16x16x32_bf16 v[102:105], v[182:185], v[210:213], v[102:105]
	v_mfma_f32_16x16x32_bf16 v[98:101], v[194:197], v[210:213], v[98:101]
	v_mfma_f32_16x16x32_bf16 v[86:89], v[182:185], v[218:221], v[86:89]
	v_mfma_f32_16x16x32_bf16 v[82:85], v[194:197], v[218:221], v[82:85]
	v_mfma_f32_16x16x32_bf16 v[70:73], v[182:185], v[226:229], v[70:73]
	v_mfma_f32_16x16x32_bf16 v[66:69], v[194:197], v[226:229], v[66:69]
	v_mfma_f32_16x16x32_bf16 v[118:121], v[190:193], v[206:209], v[118:121]
	v_mfma_f32_16x16x32_bf16 v[114:117], v[198:201], v[206:209], v[114:117]
	v_mfma_f32_16x16x32_bf16 v[102:105], v[190:193], v[214:217], v[102:105]
	v_mfma_f32_16x16x32_bf16 v[98:101], v[198:201], v[214:217], v[98:101]
	v_mfma_f32_16x16x32_bf16 v[86:89], v[190:193], v[222:225], v[86:89]
	v_mfma_f32_16x16x32_bf16 v[82:85], v[198:201], v[222:225], v[82:85]
	v_mfma_f32_16x16x32_bf16 v[70:73], v[190:193], v[230:233], v[70:73]
	v_mfma_f32_16x16x32_bf16 v[66:69], v[198:201], v[230:233], v[66:69]
	s_setprio 0
	s_barrier
	s_mov_b32 m0, s60
	v_lshl_add_u64 v[234:235], v[234:235], 0, s[10:11]
	s_add_u32 s44, s44, 0x80080
	ds_read_b128 v[202:205], v176 offset:49152
	ds_read_b128 v[206:209], v176 offset:50176
	ds_read_b128 v[210:213], v176 offset:51200
	ds_read_b128 v[214:217], v176 offset:52224
	ds_read_b128 v[218:221], v176 offset:53248
	ds_read_b128 v[222:225], v176 offset:54272
	ds_read_b128 v[226:229], v176 offset:55296
	ds_read_b128 v[230:233], v176 offset:56320
	global_load_lds_dwordx4 v[234:235], off
	v_lshl_add_u64 v[234:235], v[236:237], 0, s[10:11]
	s_mov_b32 m0, s61
	s_addc_u32 s45, s45, 0
	global_load_lds_dwordx4 v[234:235], off
	v_lshl_add_u64 v[234:235], s[44:45], 0, v[130:131]
	s_mov_b32 m0, s64
	s_nop 0
	global_load_lds_dwordx4 v[234:235], off
	v_lshl_add_u64 v[234:235], s[44:45], 0, v[136:137]
	s_mov_b32 m0, s65
	s_nop 0
	global_load_lds_dwordx4 v[234:235], off
	v_lshl_add_u64 v[234:235], v[238:239], 0, s[10:11]
	s_mov_b32 m0, s62
	s_nop 0
	global_load_lds_dwordx4 v[234:235], off
	v_lshl_add_u64 v[234:235], v[240:241], 0, s[10:11]
	s_mov_b32 m0, s63
	s_nop 0
	global_load_lds_dwordx4 v[234:235], off
	s_waitcnt vmcnt(8)
	s_waitcnt lgkmcnt(0)
	s_barrier
	s_setprio 1
	s_waitcnt lgkmcnt(0)
	v_mfma_f32_16x16x32_bf16 v[62:65], v[178:181], v[202:205], v[62:65]
	v_mfma_f32_16x16x32_bf16 v[58:61], v[154:157], v[202:205], v[58:61]
	v_mfma_f32_16x16x32_bf16 v[46:49], v[178:181], v[210:213], v[46:49]
	v_mfma_f32_16x16x32_bf16 v[42:45], v[154:157], v[210:213], v[42:45]
	v_mfma_f32_16x16x32_bf16 v[30:33], v[178:181], v[218:221], v[30:33]
	v_mfma_f32_16x16x32_bf16 v[26:29], v[154:157], v[218:221], v[26:29]
	v_mfma_f32_16x16x32_bf16 v[14:17], v[178:181], v[226:229], v[14:17]
	v_mfma_f32_16x16x32_bf16 v[10:13], v[154:157], v[226:229], v[10:13]
	v_mfma_f32_16x16x32_bf16 v[62:65], v[150:153], v[206:209], v[62:65]
	v_mfma_f32_16x16x32_bf16 v[58:61], v[186:189], v[206:209], v[58:61]
	v_mfma_f32_16x16x32_bf16 v[46:49], v[150:153], v[214:217], v[46:49]
	v_mfma_f32_16x16x32_bf16 v[42:45], v[186:189], v[214:217], v[42:45]
	v_mfma_f32_16x16x32_bf16 v[30:33], v[150:153], v[222:225], v[30:33]
	v_mfma_f32_16x16x32_bf16 v[26:29], v[186:189], v[222:225], v[26:29]
	v_mfma_f32_16x16x32_bf16 v[14:17], v[150:153], v[230:233], v[14:17]
	v_mfma_f32_16x16x32_bf16 v[10:13], v[186:189], v[230:233], v[10:13]
	s_setprio 0
	s_setprio 1
	v_mfma_f32_16x16x32_bf16 v[54:57], v[182:185], v[202:205], v[54:57]
	v_mfma_f32_16x16x32_bf16 v[50:53], v[194:197], v[202:205], v[50:53]
	v_mfma_f32_16x16x32_bf16 v[38:41], v[182:185], v[210:213], v[38:41]
	v_mfma_f32_16x16x32_bf16 v[34:37], v[194:197], v[210:213], v[34:37]
	v_mfma_f32_16x16x32_bf16 v[18:21], v[182:185], v[218:221], v[18:21]
	v_mfma_f32_16x16x32_bf16 v[22:25], v[194:197], v[218:221], v[22:25]
	v_mfma_f32_16x16x32_bf16 v[2:5], v[182:185], v[226:229], v[2:5]
	v_mfma_f32_16x16x32_bf16 v[6:9], v[194:197], v[226:229], v[6:9]
	v_mfma_f32_16x16x32_bf16 v[54:57], v[190:193], v[206:209], v[54:57]
	v_mfma_f32_16x16x32_bf16 v[50:53], v[198:201], v[206:209], v[50:53]
	v_mfma_f32_16x16x32_bf16 v[38:41], v[190:193], v[214:217], v[38:41]
	v_mfma_f32_16x16x32_bf16 v[34:37], v[198:201], v[214:217], v[34:37]
	v_mfma_f32_16x16x32_bf16 v[18:21], v[190:193], v[222:225], v[18:21]
	v_mfma_f32_16x16x32_bf16 v[22:25], v[198:201], v[222:225], v[22:25]
	v_mfma_f32_16x16x32_bf16 v[2:5], v[190:193], v[230:233], v[2:5]
	v_mfma_f32_16x16x32_bf16 v[6:9], v[198:201], v[230:233], v[6:9]
	s_setprio 0
	s_add_i32 s73, s73, 2
	s_add_u32 s42, s42, 0x100
	s_addc_u32 s43, s43, 0
	s_add_u32 s71, s71, 0x100
	s_addc_u32 s72, s72, 0
	s_cmp_gt_u32 s73, 29
	s_barrier
	s_cbranch_scc0 .LBB0_157
	s_and_b64 vcc, exec, s[12:13]
	s_cbranch_vccz .LBB0_160
	s_barrier

.LBB0_534:
	ds_read_b128 v[172:175], v156
	ds_read_b128 v[176:179], v157
	ds_read_b128 v[180:183], v152
	ds_read_b128 v[184:187], v153
	ds_read_b128 v[188:191], v158
	ds_read_b128 v[192:195], v159
	ds_read_b128 v[196:199], v160
	ds_read_b128 v[200:203], v161
	s_add_u32 s36, s34, 0x80
	s_addc_u32 s37, s35, 0
	s_cmp_eq_u32 s74, 28
	s_cselect_b32 s39, s25, s37
	s_cselect_b32 s38, s70, s36
	s_cselect_b32 s37, s23, s73
	s_cselect_b32 s36, s71, s72
	v_lshl_add_u64 v[150:151], s[34:35], 0, v[142:143]
	s_add_i32 m0, s31, 0xc000
	ds_read_b128 v[204:207], v170
	ds_read_b128 v[208:211], v170 offset:1024
	ds_read_b128 v[212:215], v170 offset:2048
	ds_read_b128 v[216:219], v170 offset:3072
	ds_read_b128 v[220:223], v170 offset:4096
	ds_read_b128 v[224:227], v170 offset:5120
	ds_read_b128 v[228:231], v170 offset:6144
	ds_read_b128 v[232:235], v170 offset:7168
	global_load_lds_dwordx4 v[150:151], off
	v_lshl_add_u64 v[150:151], s[34:35], 0, v[144:145]
	s_add_i32 m0, s31, 0xe000
	s_nop 0
	global_load_lds_dwordx4 v[150:151], off
	s_waitcnt vmcnt(8)
	s_waitcnt lgkmcnt(0)
	s_barrier
	s_setprio 1
	s_waitcnt lgkmcnt(0)
	v_mfma_f32_16x16x32_bf16 v[126:129], v[180:183], v[204:207], v[126:129]
	v_mfma_f32_16x16x32_bf16 v[122:125], v[176:179], v[204:207], v[122:125]
	v_mfma_f32_16x16x32_bf16 v[118:121], v[180:183], v[212:215], v[118:121]
	v_mfma_f32_16x16x32_bf16 v[110:113], v[176:179], v[212:215], v[110:113]
	v_mfma_f32_16x16x32_bf16 v[102:105], v[180:183], v[220:223], v[102:105]
	v_mfma_f32_16x16x32_bf16 v[94:97], v[176:179], v[220:223], v[94:97]
	v_mfma_f32_16x16x32_bf16 v[86:89], v[180:183], v[228:231], v[86:89]
	v_mfma_f32_16x16x32_bf16 v[78:81], v[176:179], v[228:231], v[78:81]
	v_mfma_f32_16x16x32_bf16 v[126:129], v[172:175], v[208:211], v[126:129]
	v_mfma_f32_16x16x32_bf16 v[122:125], v[188:191], v[208:211], v[122:125]
	v_mfma_f32_16x16x32_bf16 v[118:121], v[172:175], v[216:219], v[118:121]
	v_mfma_f32_16x16x32_bf16 v[110:113], v[188:191], v[216:219], v[110:113]
	v_mfma_f32_16x16x32_bf16 v[102:105], v[172:175], v[224:227], v[102:105]
	v_mfma_f32_16x16x32_bf16 v[94:97], v[188:191], v[224:227], v[94:97]
	v_mfma_f32_16x16x32_bf16 v[86:89], v[172:175], v[232:235], v[86:89]
	v_mfma_f32_16x16x32_bf16 v[78:81], v[188:191], v[232:235], v[78:81]
	s_setprio 0
	s_setprio 1
	v_mfma_f32_16x16x32_bf16 v[114:117], v[184:187], v[204:207], v[114:117]
	v_mfma_f32_16x16x32_bf16 v[106:109], v[196:199], v[204:207], v[106:109]
	v_mfma_f32_16x16x32_bf16 v[98:101], v[184:187], v[212:215], v[98:101]
	v_mfma_f32_16x16x32_bf16 v[90:93], v[196:199], v[212:215], v[90:93]
	v_mfma_f32_16x16x32_bf16 v[82:85], v[184:187], v[220:223], v[82:85]
	v_mfma_f32_16x16x32_bf16 v[74:77], v[196:199], v[220:223], v[74:77]
	v_mfma_f32_16x16x32_bf16 v[70:73], v[184:187], v[228:231], v[70:73]
	v_mfma_f32_16x16x32_bf16 v[66:69], v[196:199], v[228:231], v[66:69]
	v_mfma_f32_16x16x32_bf16 v[114:117], v[192:195], v[208:211], v[114:117]
	v_mfma_f32_16x16x32_bf16 v[106:109], v[200:203], v[208:211], v[106:109]
	v_mfma_f32_16x16x32_bf16 v[98:101], v[192:195], v[216:219], v[98:101]
	v_mfma_f32_16x16x32_bf16 v[90:93], v[200:203], v[216:219], v[90:93]
	v_mfma_f32_16x16x32_bf16 v[82:85], v[192:195], v[224:227], v[82:85]
	v_mfma_f32_16x16x32_bf16 v[74:77], v[200:203], v[224:227], v[74:77]
	v_mfma_f32_16x16x32_bf16 v[70:73], v[192:195], v[232:235], v[70:73]
	v_mfma_f32_16x16x32_bf16 v[66:69], v[200:203], v[232:235], v[66:69]
	s_setprio 0
	s_barrier
	s_mov_b32 m0, s42
	v_lshl_add_u64 v[150:151], s[36:37], 0, v[130:131]
	s_add_u32 s76, s36, 0x80000
	ds_read_b128 v[204:207], v170 offset:16384
	ds_read_b128 v[208:211], v170 offset:17408
	ds_read_b128 v[212:215], v170 offset:18432
	ds_read_b128 v[216:219], v170 offset:19456
	ds_read_b128 v[220:223], v170 offset:20480
	ds_read_b128 v[224:227], v170 offset:21504
	ds_read_b128 v[228:231], v170 offset:22528
	ds_read_b128 v[232:235], v170 offset:23552
	global_load_lds_dwordx4 v[150:151], off
	v_lshl_add_u64 v[236:237], s[36:37], 0, v[136:137]
	s_mov_b32 m0, s43
	s_addc_u32 s77, s37, 0
	global_load_lds_dwordx4 v[236:237], off
	v_lshl_add_u64 v[238:239], s[76:77], 0, v[130:131]
	s_mov_b32 m0, s44
	v_lshl_add_u64 v[240:241], s[38:39], 0, v[138:139]
	global_load_lds_dwordx4 v[238:239], off
	v_lshl_add_u64 v[238:239], s[76:77], 0, v[136:137]
	s_mov_b32 m0, s45
	s_nop 0
	global_load_lds_dwordx4 v[238:239], off
	v_lshl_add_u64 v[238:239], s[38:39], 0, v[132:133]
	s_mov_b32 m0, s31
	s_nop 0
	global_load_lds_dwordx4 v[238:239], off
	s_mov_b32 m0, s46
	s_nop 0
	global_load_lds_dwordx4 v[240:241], off
	s_waitcnt vmcnt(8)
	s_waitcnt lgkmcnt(0)
	s_barrier
	s_setprio 1
	s_waitcnt lgkmcnt(0)
	v_mfma_f32_16x16x32_bf16 v[62:65], v[180:183], v[204:207], v[62:65]
	v_mfma_f32_16x16x32_bf16 v[58:61], v[176:179], v[204:207], v[58:61]
	v_mfma_f32_16x16x32_bf16 v[46:49], v[180:183], v[212:215], v[46:49]
	v_mfma_f32_16x16x32_bf16 v[38:41], v[176:179], v[212:215], v[38:41]
	v_mfma_f32_16x16x32_bf16 v[22:25], v[180:183], v[220:223], v[22:25]
	v_mfma_f32_16x16x32_bf16 v[14:17], v[176:179], v[220:223], v[14:17]
	v_mfma_f32_16x16x32_bf16 v[6:9], v[180:183], v[228:231], v[6:9]
	v_mfma_f32_16x16x32_bf16 v[2:5], v[176:179], v[228:231], v[2:5]
	v_mfma_f32_16x16x32_bf16 v[62:65], v[172:175], v[208:211], v[62:65]
	v_mfma_f32_16x16x32_bf16 v[58:61], v[188:191], v[208:211], v[58:61]
	v_mfma_f32_16x16x32_bf16 v[46:49], v[172:175], v[216:219], v[46:49]
	v_mfma_f32_16x16x32_bf16 v[38:41], v[188:191], v[216:219], v[38:41]
	v_mfma_f32_16x16x32_bf16 v[22:25], v[172:175], v[224:227], v[22:25]
	v_mfma_f32_16x16x32_bf16 v[14:17], v[188:191], v[224:227], v[14:17]
	v_mfma_f32_16x16x32_bf16 v[6:9], v[172:175], v[232:235], v[6:9]
	v_mfma_f32_16x16x32_bf16 v[2:5], v[188:191], v[232:235], v[2:5]
	s_setprio 0
	s_setprio 1
	v_mfma_f32_16x16x32_bf16 v[42:45], v[184:187], v[204:207], v[42:45]
	v_mfma_f32_16x16x32_bf16 v[30:33], v[196:199], v[204:207], v[30:33]
	v_mfma_f32_16x16x32_bf16 v[18:21], v[184:187], v[212:215], v[18:21]
	v_mfma_f32_16x16x32_bf16 v[10:13], v[196:199], v[212:215], v[10:13]
	v_mfma_f32_16x16x32_bf16 v[54:57], v[184:187], v[220:223], v[54:57]
	v_mfma_f32_16x16x32_bf16 v[50:53], v[196:199], v[220:223], v[50:53]
	v_mfma_f32_16x16x32_bf16 v[34:37], v[184:187], v[228:231], v[34:37]
	v_mfma_f32_16x16x32_bf16 v[26:29], v[196:199], v[228:231], v[26:29]
	v_mfma_f32_16x16x32_bf16 v[42:45], v[192:195], v[208:211], v[42:45]
	v_mfma_f32_16x16x32_bf16 v[30:33], v[200:203], v[208:211], v[30:33]
	v_mfma_f32_16x16x32_bf16 v[18:21], v[192:195], v[216:219], v[18:21]
	v_mfma_f32_16x16x32_bf16 v[10:13], v[200:203], v[216:219], v[10:13]
	v_mfma_f32_16x16x32_bf16 v[54:57], v[192:195], v[224:227], v[54:57]
	v_mfma_f32_16x16x32_bf16 v[50:53], v[200:203], v[224:227], v[50:53]
	v_mfma_f32_16x16x32_bf16 v[34:37], v[192:195], v[232:235], v[34:37]
	v_mfma_f32_16x16x32_bf16 v[26:29], v[200:203], v[232:235], v[26:29]
	s_setprio 0
	s_barrier
	ds_read_b128 v[172:175], v163
	ds_read_b128 v[176:179], v164
	ds_read_b128 v[180:183], v154
	ds_read_b128 v[184:187], v155
	ds_read_b128 v[188:191], v165
	ds_read_b128 v[192:195], v166
	ds_read_b128 v[196:199], v167
	ds_read_b128 v[200:203], v168
	s_mov_b32 m0, s47
	v_lshl_add_u64 v[242:243], s[38:39], 0, v[134:135]
	ds_read_b128 v[204:207], v170 offset:32768
	ds_read_b128 v[208:211], v170 offset:33792
	ds_read_b128 v[212:215], v170 offset:34816
	ds_read_b128 v[216:219], v170 offset:35840
	ds_read_b128 v[220:223], v170 offset:36864
	ds_read_b128 v[224:227], v170 offset:37888
	ds_read_b128 v[228:231], v170 offset:38912
	ds_read_b128 v[232:235], v170 offset:39936
	global_load_lds_dwordx4 v[242:243], off
	v_lshl_add_u64 v[242:243], s[38:39], 0, v[140:141]
	s_mov_b32 m0, s53
	s_nop 0
	global_load_lds_dwordx4 v[242:243], off
	s_waitcnt vmcnt(8)
	s_waitcnt lgkmcnt(0)
	s_barrier
	s_setprio 1
	s_waitcnt lgkmcnt(0)
	v_mfma_f32_16x16x32_bf16 v[126:129], v[180:183], v[204:207], v[126:129]
	v_mfma_f32_16x16x32_bf16 v[122:125], v[176:179], v[204:207], v[122:125]
	v_mfma_f32_16x16x32_bf16 v[118:121], v[180:183], v[212:215], v[118:121]
	v_mfma_f32_16x16x32_bf16 v[110:113], v[176:179], v[212:215], v[110:113]
	v_mfma_f32_16x16x32_bf16 v[102:105], v[180:183], v[220:223], v[102:105]
	v_mfma_f32_16x16x32_bf16 v[94:97], v[176:179], v[220:223], v[94:97]
	v_mfma_f32_16x16x32_bf16 v[86:89], v[180:183], v[228:231], v[86:89]
	v_mfma_f32_16x16x32_bf16 v[78:81], v[176:179], v[228:231], v[78:81]
	v_mfma_f32_16x16x32_bf16 v[126:129], v[172:175], v[208:211], v[126:129]
	v_mfma_f32_16x16x32_bf16 v[122:125], v[188:191], v[208:211], v[122:125]
	v_mfma_f32_16x16x32_bf16 v[118:121], v[172:175], v[216:219], v[118:121]
	v_mfma_f32_16x16x32_bf16 v[110:113], v[188:191], v[216:219], v[110:113]
	v_mfma_f32_16x16x32_bf16 v[102:105], v[172:175], v[224:227], v[102:105]
	v_mfma_f32_16x16x32_bf16 v[94:97], v[188:191], v[224:227], v[94:97]
	v_mfma_f32_16x16x32_bf16 v[86:89], v[172:175], v[232:235], v[86:89]
	v_mfma_f32_16x16x32_bf16 v[78:81], v[188:191], v[232:235], v[78:81]
	s_setprio 0
	s_setprio 1
	v_mfma_f32_16x16x32_bf16 v[114:117], v[184:187], v[204:207], v[114:117]
	v_mfma_f32_16x16x32_bf16 v[106:109], v[196:199], v[204:207], v[106:109]
	v_mfma_f32_16x16x32_bf16 v[98:101], v[184:187], v[212:215], v[98:101]
	v_mfma_f32_16x16x32_bf16 v[90:93], v[196:199], v[212:215], v[90:93]
	v_mfma_f32_16x16x32_bf16 v[82:85], v[184:187], v[220:223], v[82:85]
	v_mfma_f32_16x16x32_bf16 v[74:77], v[196:199], v[220:223], v[74:77]
	v_mfma_f32_16x16x32_bf16 v[70:73], v[184:187], v[228:231], v[70:73]
	v_mfma_f32_16x16x32_bf16 v[66:69], v[196:199], v[228:231], v[66:69]
	v_mfma_f32_16x16x32_bf16 v[114:117], v[192:195], v[208:211], v[114:117]
	v_mfma_f32_16x16x32_bf16 v[106:109], v[200:203], v[208:211], v[106:109]
	v_mfma_f32_16x16x32_bf16 v[98:101], v[192:195], v[216:219], v[98:101]
	v_mfma_f32_16x16x32_bf16 v[90:93], v[200:203], v[216:219], v[90:93]
	v_mfma_f32_16x16x32_bf16 v[82:85], v[192:195], v[224:227], v[82:85]
	v_mfma_f32_16x16x32_bf16 v[74:77], v[200:203], v[224:227], v[74:77]
	v_mfma_f32_16x16x32_bf16 v[70:73], v[192:195], v[232:235], v[70:73]
	v_mfma_f32_16x16x32_bf16 v[66:69], v[200:203], v[232:235], v[66:69]
	s_setprio 0
	s_barrier
	s_mov_b32 m0, s59
	v_lshl_add_u64 v[150:151], v[150:151], 0, s[12:13]
	s_add_u32 s36, s36, 0x80080
	ds_read_b128 v[204:207], v170 offset:49152
	ds_read_b128 v[208:211], v170 offset:50176
	ds_read_b128 v[212:215], v170 offset:51200
	ds_read_b128 v[216:219], v170 offset:52224
	ds_read_b128 v[220:223], v170 offset:53248
	ds_read_b128 v[224:227], v170 offset:54272
	ds_read_b128 v[228:231], v170 offset:55296
	ds_read_b128 v[232:235], v170 offset:56320
	global_load_lds_dwordx4 v[150:151], off
	v_lshl_add_u64 v[150:151], v[236:237], 0, s[12:13]
	s_mov_b32 m0, s60
	s_addc_u32 s37, s37, 0
	global_load_lds_dwordx4 v[150:151], off
	v_lshl_add_u64 v[150:151], s[36:37], 0, v[130:131]
	s_mov_b32 m0, s63
	s_nop 0
	global_load_lds_dwordx4 v[150:151], off
	v_lshl_add_u64 v[150:151], s[36:37], 0, v[136:137]
	s_mov_b32 m0, s64
	s_nop 0
	global_load_lds_dwordx4 v[150:151], off
	v_lshl_add_u64 v[150:151], v[238:239], 0, s[12:13]
	s_mov_b32 m0, s61
	s_nop 0
	global_load_lds_dwordx4 v[150:151], off
	v_lshl_add_u64 v[150:151], v[240:241], 0, s[12:13]
	s_mov_b32 m0, s62
	s_nop 0
	global_load_lds_dwordx4 v[150:151], off
	s_waitcnt vmcnt(8)
	s_waitcnt lgkmcnt(0)
	s_barrier
	s_setprio 1
	s_waitcnt lgkmcnt(0)
	v_mfma_f32_16x16x32_bf16 v[62:65], v[180:183], v[204:207], v[62:65]
	v_mfma_f32_16x16x32_bf16 v[58:61], v[176:179], v[204:207], v[58:61]
	v_mfma_f32_16x16x32_bf16 v[46:49], v[180:183], v[212:215], v[46:49]
	v_mfma_f32_16x16x32_bf16 v[38:41], v[176:179], v[212:215], v[38:41]
	v_mfma_f32_16x16x32_bf16 v[22:25], v[180:183], v[220:223], v[22:25]
	v_mfma_f32_16x16x32_bf16 v[14:17], v[176:179], v[220:223], v[14:17]
	v_mfma_f32_16x16x32_bf16 v[6:9], v[180:183], v[228:231], v[6:9]
	v_mfma_f32_16x16x32_bf16 v[2:5], v[176:179], v[228:231], v[2:5]
	v_mfma_f32_16x16x32_bf16 v[62:65], v[172:175], v[208:211], v[62:65]
	v_mfma_f32_16x16x32_bf16 v[58:61], v[188:191], v[208:211], v[58:61]
	v_mfma_f32_16x16x32_bf16 v[46:49], v[172:175], v[216:219], v[46:49]
	v_mfma_f32_16x16x32_bf16 v[38:41], v[188:191], v[216:219], v[38:41]
	v_mfma_f32_16x16x32_bf16 v[22:25], v[172:175], v[224:227], v[22:25]
	v_mfma_f32_16x16x32_bf16 v[14:17], v[188:191], v[224:227], v[14:17]
	v_mfma_f32_16x16x32_bf16 v[6:9], v[172:175], v[232:235], v[6:9]
	v_mfma_f32_16x16x32_bf16 v[2:5], v[188:191], v[232:235], v[2:5]
	s_setprio 0
	s_setprio 1
	v_mfma_f32_16x16x32_bf16 v[42:45], v[184:187], v[204:207], v[42:45]
	v_mfma_f32_16x16x32_bf16 v[30:33], v[196:199], v[204:207], v[30:33]
	v_mfma_f32_16x16x32_bf16 v[18:21], v[184:187], v[212:215], v[18:21]
	v_mfma_f32_16x16x32_bf16 v[10:13], v[196:199], v[212:215], v[10:13]
	v_mfma_f32_16x16x32_bf16 v[54:57], v[184:187], v[220:223], v[54:57]
	v_mfma_f32_16x16x32_bf16 v[50:53], v[196:199], v[220:223], v[50:53]
	v_mfma_f32_16x16x32_bf16 v[34:37], v[184:187], v[228:231], v[34:37]
	v_mfma_f32_16x16x32_bf16 v[26:29], v[196:199], v[228:231], v[26:29]
	v_mfma_f32_16x16x32_bf16 v[42:45], v[192:195], v[208:211], v[42:45]
	v_mfma_f32_16x16x32_bf16 v[30:33], v[200:203], v[208:211], v[30:33]
	v_mfma_f32_16x16x32_bf16 v[18:21], v[192:195], v[216:219], v[18:21]
	v_mfma_f32_16x16x32_bf16 v[10:13], v[200:203], v[216:219], v[10:13]
	v_mfma_f32_16x16x32_bf16 v[54:57], v[192:195], v[224:227], v[54:57]
	v_mfma_f32_16x16x32_bf16 v[50:53], v[200:203], v[224:227], v[50:53]
	v_mfma_f32_16x16x32_bf16 v[34:37], v[192:195], v[232:235], v[34:37]
	v_mfma_f32_16x16x32_bf16 v[26:29], v[200:203], v[232:235], v[26:29]
	s_setprio 0
	s_add_i32 s74, s74, 2
	s_add_u32 s34, s34, 0x100
	s_addc_u32 s35, s35, 0
	s_add_u32 s72, s72, 0x100
	s_addc_u32 s73, s73, 0
	s_cmp_gt_u32 s74, 29
	s_barrier
	s_cbranch_scc0 .LBB0_534
	s_and_b64 vcc, exec, s[14:15]
	s_cbranch_vccz .LBB0_537
	s_barrier

.LBB0_727:
	ds_read_b128 v[18:21], v192
	ds_read_b128 v[22:25], v193
	ds_read_b128 v[26:29], v194
	ds_read_b128 v[30:33], v195
	ds_read_b128 v[2:5], v196
	ds_read_b128 v[6:9], v197
	ds_read_b128 v[10:13], v198
	ds_read_b128 v[14:17], v199
	s_add_u32 s42, s16, s40
	s_addc_u32 s43, s17, s41
	s_add_u32 s44, s42, 0x2600100
	s_addc_u32 s45, s43, 0
	s_add_u32 s82, s31, s40
	s_addc_u32 s83, s35, s41
	s_cmpk_eq_i32 s40, 0x700
	s_cselect_b64 vcc, -1, 0
	s_and_b64 s[42:43], vcc, exec
	v_cndmask_b32_e32 v168, v215, v214, vcc
	s_cselect_b32 s45, s19, s45
	s_cselect_b32 s44, s18, s44
	v_cndmask_b32_e32 v184, v170, v213, vcc
	v_cndmask_b32_e32 v173, v172, v212, vcc
	v_cndmask_b32_e32 v175, v174, v211, vcc
	s_cselect_b32 s43, s37, s83
	s_cselect_b32 s42, s36, s82
	v_lshl_add_u64 v[180:181], v[178:179], 0, s[40:41]
	s_add_i32 m0, s59, 0xc000
	ds_read_b128 v[216:219], v209
	ds_read_b128 v[220:223], v209 offset:1024
	ds_read_b128 v[224:227], v209 offset:2048
	ds_read_b128 v[228:231], v209 offset:3072
	ds_read_b128 v[232:235], v209 offset:4096
	ds_read_b128 v[236:239], v209 offset:5120
	ds_read_b128 v[240:243], v209 offset:6144
	ds_read_b128 v[244:247], v209 offset:7168
	global_load_lds_dwordx4 v[180:181], off
	v_lshl_add_u64 v[180:181], v[176:177], 0, s[40:41]
	s_add_i32 m0, s59, 0xe000
	s_nop 0
	global_load_lds_dwordx4 v[180:181], off
	s_waitcnt vmcnt(8)
	s_waitcnt lgkmcnt(0)
	s_barrier
	s_setprio 1
	s_waitcnt lgkmcnt(0)
	v_mfma_f32_16x16x128_f8f6f4 v[158:161], v[18:25], v[216:223], v[158:161]
	v_mfma_f32_16x16x128_f8f6f4 v[150:153], v[26:33], v[216:223], v[150:153]
	v_mfma_f32_16x16x128_f8f6f4 v[142:145], v[18:25], v[224:231], v[142:145]
	v_mfma_f32_16x16x128_f8f6f4 v[134:137], v[26:33], v[224:231], v[134:137]
	v_mfma_f32_16x16x128_f8f6f4 v[126:129], v[18:25], v[232:239], v[126:129]
	v_mfma_f32_16x16x128_f8f6f4 v[118:121], v[26:33], v[232:239], v[118:121]
	v_mfma_f32_16x16x128_f8f6f4 v[110:113], v[18:25], v[240:247], v[110:113]
	v_mfma_f32_16x16x128_f8f6f4 v[102:105], v[26:33], v[240:247], v[102:105]
	s_setprio 0
	s_setprio 1
	v_mfma_f32_16x16x128_f8f6f4 v[154:157], v[2:9], v[216:223], v[154:157]
	v_mfma_f32_16x16x128_f8f6f4 v[146:149], v[10:17], v[216:223], v[146:149]
	v_mfma_f32_16x16x128_f8f6f4 v[138:141], v[2:9], v[224:231], v[138:141]
	v_mfma_f32_16x16x128_f8f6f4 v[130:133], v[10:17], v[224:231], v[130:133]
	v_mfma_f32_16x16x128_f8f6f4 v[122:125], v[2:9], v[232:239], v[122:125]
	v_mfma_f32_16x16x128_f8f6f4 v[114:117], v[10:17], v[232:239], v[114:117]
	v_mfma_f32_16x16x128_f8f6f4 v[106:109], v[2:9], v[240:247], v[106:109]
	v_mfma_f32_16x16x128_f8f6f4 v[98:101], v[10:17], v[240:247], v[98:101]
	s_setprio 0
	s_barrier
	s_mov_b32 m0, s60
	v_lshl_add_u64 v[180:181], s[42:43], 0, v[166:167]
	s_add_u32 s82, s42, 0x40000
	ds_read_b128 v[216:219], v209 offset:16384
	ds_read_b128 v[220:223], v209 offset:17408
	ds_read_b128 v[224:227], v209 offset:18432
	ds_read_b128 v[228:231], v209 offset:19456
	ds_read_b128 v[232:235], v209 offset:20480
	ds_read_b128 v[236:239], v209 offset:21504
	ds_read_b128 v[240:243], v209 offset:22528
	ds_read_b128 v[244:247], v209 offset:23552
	global_load_lds_dwordx4 v[180:181], off
	v_lshl_add_u64 v[182:183], s[42:43], 0, v[164:165]
	s_mov_b32 m0, s61
	s_addc_u32 s83, s43, 0
	global_load_lds_dwordx4 v[182:183], off
	v_lshl_add_u64 v[186:187], s[82:83], 0, v[166:167]
	s_mov_b32 m0, s62
	v_mov_b32_e32 v185, v169
	global_load_lds_dwordx4 v[186:187], off
	v_lshl_add_u64 v[186:187], s[82:83], 0, v[164:165]
	s_mov_b32 m0, s63
	s_nop 0
	global_load_lds_dwordx4 v[186:187], off
	s_mov_b32 m0, s59
	v_lshl_add_u64 v[186:187], s[44:45], 0, v[168:169]
	global_load_lds_dwordx4 v168, s[44:45]
	s_mov_b32 m0, s64
	s_nop 0
	global_load_lds_dwordx4 v184, s[44:45]
	s_waitcnt vmcnt(8)
	s_waitcnt lgkmcnt(0)
	v_lshl_add_u64 v[184:185], s[44:45], 0, v[184:185]
	s_barrier
	s_setprio 1
	s_waitcnt lgkmcnt(0)
	v_mfma_f32_16x16x128_f8f6f4 v[94:97], v[18:25], v[216:223], v[94:97]
	v_mfma_f32_16x16x128_f8f6f4 v[86:89], v[26:33], v[216:223], v[86:89]
	v_mfma_f32_16x16x128_f8f6f4 v[78:81], v[18:25], v[224:231], v[78:81]
	v_mfma_f32_16x16x128_f8f6f4 v[70:73], v[26:33], v[224:231], v[70:73]
	v_mfma_f32_16x16x128_f8f6f4 v[62:65], v[18:25], v[232:239], v[62:65]
	v_mfma_f32_16x16x128_f8f6f4 v[54:57], v[26:33], v[232:239], v[54:57]
	v_mfma_f32_16x16x128_f8f6f4 v[46:49], v[18:25], v[240:247], v[46:49]
	v_mfma_f32_16x16x128_f8f6f4 v[38:41], v[26:33], v[240:247], v[38:41]
	s_setprio 0
	s_setprio 1
	v_mfma_f32_16x16x128_f8f6f4 v[90:93], v[2:9], v[216:223], v[90:93]
	v_mfma_f32_16x16x128_f8f6f4 v[82:85], v[10:17], v[216:223], v[82:85]
	v_mfma_f32_16x16x128_f8f6f4 v[74:77], v[2:9], v[224:231], v[74:77]
	v_mfma_f32_16x16x128_f8f6f4 v[66:69], v[10:17], v[224:231], v[66:69]
	v_mfma_f32_16x16x128_f8f6f4 v[58:61], v[2:9], v[232:239], v[58:61]
	v_mfma_f32_16x16x128_f8f6f4 v[50:53], v[10:17], v[232:239], v[50:53]
	v_mfma_f32_16x16x128_f8f6f4 v[42:45], v[2:9], v[240:247], v[42:45]
	v_mfma_f32_16x16x128_f8f6f4 v[34:37], v[10:17], v[240:247], v[34:37]
	s_setprio 0
	s_barrier
	ds_read_b128 v[2:5], v200
	ds_read_b128 v[6:9], v201
	ds_read_b128 v[10:13], v202
	ds_read_b128 v[14:17], v203
	ds_read_b128 v[18:21], v204
	ds_read_b128 v[22:25], v205
	ds_read_b128 v[26:29], v206
	ds_read_b128 v[30:33], v207
	s_mov_b32 m0, s65
	ds_read_b128 v[216:219], v209 offset:32768
	ds_read_b128 v[220:223], v209 offset:33792
	ds_read_b128 v[224:227], v209 offset:34816
	ds_read_b128 v[228:231], v209 offset:35840
	ds_read_b128 v[232:235], v209 offset:36864
	ds_read_b128 v[236:239], v209 offset:37888
	ds_read_b128 v[240:243], v209 offset:38912
	ds_read_b128 v[244:247], v209 offset:39936
	global_load_lds_dwordx4 v173, s[44:45]
	s_mov_b32 m0, s66
	s_nop 0
	global_load_lds_dwordx4 v175, s[44:45]
	s_waitcnt vmcnt(8)
	s_waitcnt lgkmcnt(0)
	s_barrier
	s_setprio 1
	s_waitcnt lgkmcnt(0)
	v_mfma_f32_16x16x128_f8f6f4 v[158:161], v[2:9], v[216:223], v[158:161]
	v_mfma_f32_16x16x128_f8f6f4 v[150:153], v[10:17], v[216:223], v[150:153]
	v_mfma_f32_16x16x128_f8f6f4 v[142:145], v[2:9], v[224:231], v[142:145]
	v_mfma_f32_16x16x128_f8f6f4 v[134:137], v[10:17], v[224:231], v[134:137]
	v_mfma_f32_16x16x128_f8f6f4 v[126:129], v[2:9], v[232:239], v[126:129]
	v_mfma_f32_16x16x128_f8f6f4 v[118:121], v[10:17], v[232:239], v[118:121]
	v_mfma_f32_16x16x128_f8f6f4 v[110:113], v[2:9], v[240:247], v[110:113]
	v_mfma_f32_16x16x128_f8f6f4 v[102:105], v[10:17], v[240:247], v[102:105]
	s_setprio 0
	s_setprio 1
	v_mfma_f32_16x16x128_f8f6f4 v[154:157], v[18:25], v[216:223], v[154:157]
	v_mfma_f32_16x16x128_f8f6f4 v[146:149], v[26:33], v[216:223], v[146:149]
	v_mfma_f32_16x16x128_f8f6f4 v[138:141], v[18:25], v[224:231], v[138:141]
	v_mfma_f32_16x16x128_f8f6f4 v[130:133], v[26:33], v[224:231], v[130:133]
	v_mfma_f32_16x16x128_f8f6f4 v[122:125], v[18:25], v[232:239], v[122:125]
	v_mfma_f32_16x16x128_f8f6f4 v[114:117], v[26:33], v[232:239], v[114:117]
	v_mfma_f32_16x16x128_f8f6f4 v[106:109], v[18:25], v[240:247], v[106:109]
	v_mfma_f32_16x16x128_f8f6f4 v[98:101], v[26:33], v[240:247], v[98:101]
	s_setprio 0
	s_barrier
	s_mov_b32 m0, s67
	v_lshl_add_u64 v[180:181], v[180:181], 0, s[24:25]
	s_add_u32 s42, s42, 0x40080
	ds_read_b128 v[216:219], v209 offset:49152
	ds_read_b128 v[220:223], v209 offset:50176
	ds_read_b128 v[224:227], v209 offset:51200
	ds_read_b128 v[228:231], v209 offset:52224
	ds_read_b128 v[232:235], v209 offset:53248
	ds_read_b128 v[236:239], v209 offset:54272
	ds_read_b128 v[240:243], v209 offset:55296
	ds_read_b128 v[244:247], v209 offset:56320
	global_load_lds_dwordx4 v[180:181], off
	v_lshl_add_u64 v[180:181], v[182:183], 0, s[24:25]
	s_mov_b32 m0, s68
	s_addc_u32 s43, s43, 0
	global_load_lds_dwordx4 v[180:181], off
	v_lshl_add_u64 v[180:181], s[42:43], 0, v[166:167]
	s_mov_b32 m0, s71
	s_nop 0
	global_load_lds_dwordx4 v[180:181], off
	v_lshl_add_u64 v[180:181], s[42:43], 0, v[164:165]
	s_mov_b32 m0, s72
	s_nop 0
	global_load_lds_dwordx4 v[180:181], off
	v_lshl_add_u64 v[180:181], v[186:187], 0, s[24:25]
	s_mov_b32 m0, s69
	s_nop 0
	global_load_lds_dwordx4 v[180:181], off
	v_lshl_add_u64 v[180:181], v[184:185], 0, s[24:25]
	s_mov_b32 m0, s70
	s_nop 0
	global_load_lds_dwordx4 v[180:181], off
	s_waitcnt vmcnt(8)
	s_waitcnt lgkmcnt(0)
	s_barrier
	s_setprio 1
	s_waitcnt lgkmcnt(0)
	v_mfma_f32_16x16x128_f8f6f4 v[94:97], v[2:9], v[216:223], v[94:97]
	v_mfma_f32_16x16x128_f8f6f4 v[86:89], v[10:17], v[216:223], v[86:89]
	v_mfma_f32_16x16x128_f8f6f4 v[78:81], v[2:9], v[224:231], v[78:81]
	v_mfma_f32_16x16x128_f8f6f4 v[70:73], v[10:17], v[224:231], v[70:73]
	v_mfma_f32_16x16x128_f8f6f4 v[62:65], v[2:9], v[232:239], v[62:65]
	v_mfma_f32_16x16x128_f8f6f4 v[54:57], v[10:17], v[232:239], v[54:57]
	v_mfma_f32_16x16x128_f8f6f4 v[46:49], v[2:9], v[240:247], v[46:49]
	v_mfma_f32_16x16x128_f8f6f4 v[38:41], v[10:17], v[240:247], v[38:41]
	s_setprio 0
	s_setprio 1
	v_mfma_f32_16x16x128_f8f6f4 v[90:93], v[18:25], v[216:223], v[90:93]
	v_mfma_f32_16x16x128_f8f6f4 v[82:85], v[26:33], v[216:223], v[82:85]
	v_mfma_f32_16x16x128_f8f6f4 v[74:77], v[18:25], v[224:231], v[74:77]
	v_mfma_f32_16x16x128_f8f6f4 v[66:69], v[26:33], v[224:231], v[66:69]
	v_mfma_f32_16x16x128_f8f6f4 v[58:61], v[18:25], v[232:239], v[58:61]
	v_mfma_f32_16x16x128_f8f6f4 v[50:53], v[26:33], v[232:239], v[50:53]
	v_mfma_f32_16x16x128_f8f6f4 v[42:45], v[18:25], v[240:247], v[42:45]
	v_mfma_f32_16x16x128_f8f6f4 v[34:37], v[26:33], v[240:247], v[34:37]
	s_setprio 0
	s_add_i32 s81, s81, 2
	s_add_u32 s40, s40, 0x100
	s_addc_u32 s41, s41, 0
	s_cmp_gt_u32 s81, 13
	s_barrier
	s_cbranch_scc0 .LBB0_727
	s_and_b64 vcc, exec, s[28:29]
	s_cbranch_vccz .LBB0_730
	s_barrier

.LBB0_831:
	ds_read_b128 v[18:21], v188
	ds_read_b128 v[22:25], v189
	ds_read_b128 v[26:29], v190
	ds_read_b128 v[30:33], v191
	ds_read_b128 v[2:5], v192
	ds_read_b128 v[6:9], v193
	ds_read_b128 v[10:13], v194
	ds_read_b128 v[14:17], v195
	s_add_u32 s64, s62, 0x80
	s_addc_u32 s65, s63, 0
	s_cmp_eq_u32 s91, 12
	s_cselect_b32 s67, s17, s65
	s_cselect_b32 s66, s39, s64
	s_cselect_b32 s65, s43, s90
	s_cselect_b32 s64, s42, s41
	v_lshl_add_u64 v[232:233], s[62:63], 0, v[176:177]
	s_add_i32 m0, s61, 0xc000
	ds_read_b128 v[180:183], v206
	ds_read_b128 v[184:187], v206 offset:1024
	ds_read_b128 v[208:211], v206 offset:2048
	ds_read_b128 v[212:215], v206 offset:3072
	ds_read_b128 v[216:219], v206 offset:4096
	ds_read_b128 v[220:223], v206 offset:5120
	ds_read_b128 v[224:227], v206 offset:6144
	ds_read_b128 v[228:231], v206 offset:7168
	global_load_lds_dwordx4 v[232:233], off
	v_lshl_add_u64 v[232:233], s[62:63], 0, v[178:179]
	s_add_i32 m0, s61, 0xe000
	s_nop 0
	global_load_lds_dwordx4 v[232:233], off
	s_waitcnt vmcnt(8)
	s_waitcnt lgkmcnt(0)
	s_barrier
	s_setprio 1
	s_waitcnt lgkmcnt(0)
	v_mfma_f32_16x16x128_f8f6f4 v[158:161], v[18:25], v[180:187], v[158:161]
	v_mfma_f32_16x16x128_f8f6f4 v[154:157], v[26:33], v[180:187], v[154:157]
	v_mfma_f32_16x16x128_f8f6f4 v[146:149], v[18:25], v[208:215], v[146:149]
	v_mfma_f32_16x16x128_f8f6f4 v[138:141], v[26:33], v[208:215], v[138:141]
	v_mfma_f32_16x16x128_f8f6f4 v[130:133], v[18:25], v[216:223], v[130:133]
	v_mfma_f32_16x16x128_f8f6f4 v[122:125], v[26:33], v[216:223], v[122:125]
	v_mfma_f32_16x16x128_f8f6f4 v[114:117], v[18:25], v[224:231], v[114:117]
	v_mfma_f32_16x16x128_f8f6f4 v[106:109], v[26:33], v[224:231], v[106:109]
	s_setprio 0
	s_setprio 1
	v_mfma_f32_16x16x128_f8f6f4 v[150:153], v[2:9], v[180:187], v[150:153]
	v_mfma_f32_16x16x128_f8f6f4 v[142:145], v[10:17], v[180:187], v[142:145]
	v_mfma_f32_16x16x128_f8f6f4 v[134:137], v[2:9], v[208:215], v[134:137]
	v_mfma_f32_16x16x128_f8f6f4 v[126:129], v[10:17], v[208:215], v[126:129]
	v_mfma_f32_16x16x128_f8f6f4 v[118:121], v[2:9], v[216:223], v[118:121]
	v_mfma_f32_16x16x128_f8f6f4 v[110:113], v[10:17], v[216:223], v[110:113]
	v_mfma_f32_16x16x128_f8f6f4 v[102:105], v[2:9], v[224:231], v[102:105]
	v_mfma_f32_16x16x128_f8f6f4 v[98:101], v[10:17], v[224:231], v[98:101]
	s_setprio 0
	s_barrier
	s_mov_b32 m0, s68
	v_lshl_add_u64 v[180:181], s[64:65], 0, v[164:165]
	s_add_u32 s92, s64, 0x40000
	ds_read_b128 v[208:211], v206 offset:16384
	ds_read_b128 v[212:215], v206 offset:17408
	ds_read_b128 v[216:219], v206 offset:18432
	ds_read_b128 v[220:223], v206 offset:19456
	ds_read_b128 v[224:227], v206 offset:20480
	ds_read_b128 v[228:231], v206 offset:21504
	ds_read_b128 v[232:235], v206 offset:22528
	ds_read_b128 v[236:239], v206 offset:23552
	global_load_lds_dwordx4 v[180:181], off
	v_lshl_add_u64 v[182:183], s[64:65], 0, v[170:171]
	s_mov_b32 m0, s69
	s_addc_u32 s93, s65, 0
	global_load_lds_dwordx4 v[182:183], off
	v_lshl_add_u64 v[184:185], s[92:93], 0, v[164:165]
	s_mov_b32 m0, s70
	v_lshl_add_u64 v[186:187], s[66:67], 0, v[172:173]
	global_load_lds_dwordx4 v[184:185], off
	v_lshl_add_u64 v[184:185], s[92:93], 0, v[170:171]
	s_mov_b32 m0, s71
	s_nop 0
	global_load_lds_dwordx4 v[184:185], off
	v_lshl_add_u64 v[184:185], s[66:67], 0, v[166:167]
	s_mov_b32 m0, s61
	s_nop 0
	global_load_lds_dwordx4 v[184:185], off
	s_mov_b32 m0, s72
	s_nop 0
	global_load_lds_dwordx4 v[186:187], off
	s_waitcnt vmcnt(8)
	s_waitcnt lgkmcnt(0)
	s_barrier
	s_setprio 1
	s_waitcnt lgkmcnt(0)
	v_mfma_f32_16x16x128_f8f6f4 v[94:97], v[18:25], v[208:215], v[94:97]
	v_mfma_f32_16x16x128_f8f6f4 v[90:93], v[26:33], v[208:215], v[90:93]
	v_mfma_f32_16x16x128_f8f6f4 v[82:85], v[18:25], v[216:223], v[82:85]
	v_mfma_f32_16x16x128_f8f6f4 v[70:73], v[26:33], v[216:223], v[70:73]
	v_mfma_f32_16x16x128_f8f6f4 v[58:61], v[18:25], v[224:231], v[58:61]
	v_mfma_f32_16x16x128_f8f6f4 v[42:45], v[26:33], v[224:231], v[42:45]
	v_mfma_f32_16x16x128_f8f6f4 v[38:41], v[18:25], v[232:239], v[38:41]
	v_mfma_f32_16x16x128_f8f6f4 v[34:37], v[26:33], v[232:239], v[34:37]
	s_setprio 0
	s_setprio 1
	v_mfma_f32_16x16x128_f8f6f4 v[86:89], v[2:9], v[208:215], v[86:89]
	v_mfma_f32_16x16x128_f8f6f4 v[78:81], v[10:17], v[208:215], v[78:81]
	v_mfma_f32_16x16x128_f8f6f4 v[62:65], v[2:9], v[216:223], v[62:65]
	v_mfma_f32_16x16x128_f8f6f4 v[46:49], v[10:17], v[216:223], v[46:49]
	v_mfma_f32_16x16x128_f8f6f4 v[74:77], v[2:9], v[224:231], v[74:77]
	v_mfma_f32_16x16x128_f8f6f4 v[66:69], v[10:17], v[224:231], v[66:69]
	v_mfma_f32_16x16x128_f8f6f4 v[54:57], v[2:9], v[232:239], v[54:57]
	v_mfma_f32_16x16x128_f8f6f4 v[50:53], v[10:17], v[232:239], v[50:53]
	s_setprio 0
	s_barrier
	ds_read_b128 v[2:5], v196
	ds_read_b128 v[6:9], v197
	ds_read_b128 v[10:13], v198
	ds_read_b128 v[14:17], v199
	ds_read_b128 v[18:21], v200
	ds_read_b128 v[22:25], v201
	ds_read_b128 v[26:29], v202
	ds_read_b128 v[30:33], v203
	s_mov_b32 m0, s73
	v_lshl_add_u64 v[240:241], s[66:67], 0, v[168:169]
	ds_read_b128 v[208:211], v206 offset:32768
	ds_read_b128 v[212:215], v206 offset:33792
	ds_read_b128 v[216:219], v206 offset:34816
	ds_read_b128 v[220:223], v206 offset:35840
	ds_read_b128 v[224:227], v206 offset:36864
	ds_read_b128 v[228:231], v206 offset:37888
	ds_read_b128 v[232:235], v206 offset:38912
	ds_read_b128 v[236:239], v206 offset:39936
	global_load_lds_dwordx4 v[240:241], off
	v_lshl_add_u64 v[240:241], s[66:67], 0, v[174:175]
	s_mov_b32 m0, s74
	s_nop 0
	global_load_lds_dwordx4 v[240:241], off
	s_waitcnt vmcnt(8)
	s_waitcnt lgkmcnt(0)
	s_barrier
	s_setprio 1
	s_waitcnt lgkmcnt(0)
	v_mfma_f32_16x16x128_f8f6f4 v[158:161], v[2:9], v[208:215], v[158:161]
	v_mfma_f32_16x16x128_f8f6f4 v[154:157], v[10:17], v[208:215], v[154:157]
	v_mfma_f32_16x16x128_f8f6f4 v[146:149], v[2:9], v[216:223], v[146:149]
	v_mfma_f32_16x16x128_f8f6f4 v[138:141], v[10:17], v[216:223], v[138:141]
	v_mfma_f32_16x16x128_f8f6f4 v[130:133], v[2:9], v[224:231], v[130:133]
	v_mfma_f32_16x16x128_f8f6f4 v[122:125], v[10:17], v[224:231], v[122:125]
	v_mfma_f32_16x16x128_f8f6f4 v[114:117], v[2:9], v[232:239], v[114:117]
	v_mfma_f32_16x16x128_f8f6f4 v[106:109], v[10:17], v[232:239], v[106:109]
	s_setprio 0
	s_setprio 1
	v_mfma_f32_16x16x128_f8f6f4 v[150:153], v[18:25], v[208:215], v[150:153]
	v_mfma_f32_16x16x128_f8f6f4 v[142:145], v[26:33], v[208:215], v[142:145]
	v_mfma_f32_16x16x128_f8f6f4 v[134:137], v[18:25], v[216:223], v[134:137]
	v_mfma_f32_16x16x128_f8f6f4 v[126:129], v[26:33], v[216:223], v[126:129]
	v_mfma_f32_16x16x128_f8f6f4 v[118:121], v[18:25], v[224:231], v[118:121]
	v_mfma_f32_16x16x128_f8f6f4 v[110:113], v[26:33], v[224:231], v[110:113]
	v_mfma_f32_16x16x128_f8f6f4 v[102:105], v[18:25], v[232:239], v[102:105]
	v_mfma_f32_16x16x128_f8f6f4 v[98:101], v[26:33], v[232:239], v[98:101]
	s_setprio 0
	s_barrier
	s_mov_b32 m0, s79
	v_lshl_add_u64 v[180:181], v[180:181], 0, s[24:25]
	s_add_u32 s64, s64, 0x40080
	ds_read_b128 v[208:211], v206 offset:49152
	ds_read_b128 v[212:215], v206 offset:50176
	ds_read_b128 v[216:219], v206 offset:51200
	ds_read_b128 v[220:223], v206 offset:52224
	ds_read_b128 v[224:227], v206 offset:53248
	ds_read_b128 v[228:231], v206 offset:54272
	ds_read_b128 v[232:235], v206 offset:55296
	ds_read_b128 v[236:239], v206 offset:56320
	global_load_lds_dwordx4 v[180:181], off
	v_lshl_add_u64 v[180:181], v[182:183], 0, s[24:25]
	s_mov_b32 m0, s80
	s_addc_u32 s65, s65, 0
	global_load_lds_dwordx4 v[180:181], off
	v_lshl_add_u64 v[180:181], s[64:65], 0, v[164:165]
	s_mov_b32 m0, s83
	s_nop 0
	global_load_lds_dwordx4 v[180:181], off
	v_lshl_add_u64 v[180:181], s[64:65], 0, v[170:171]
	s_mov_b32 m0, s84
	s_nop 0
	global_load_lds_dwordx4 v[180:181], off
	v_lshl_add_u64 v[180:181], v[184:185], 0, s[24:25]
	s_mov_b32 m0, s81
	s_nop 0
	global_load_lds_dwordx4 v[180:181], off
	v_lshl_add_u64 v[180:181], v[186:187], 0, s[24:25]
	s_mov_b32 m0, s82
	s_nop 0
	global_load_lds_dwordx4 v[180:181], off
	s_waitcnt vmcnt(8)
	s_waitcnt lgkmcnt(0)
	s_barrier
	s_setprio 1
	s_waitcnt lgkmcnt(0)
	v_mfma_f32_16x16x128_f8f6f4 v[94:97], v[2:9], v[208:215], v[94:97]
	v_mfma_f32_16x16x128_f8f6f4 v[90:93], v[10:17], v[208:215], v[90:93]
	v_mfma_f32_16x16x128_f8f6f4 v[82:85], v[2:9], v[216:223], v[82:85]
	v_mfma_f32_16x16x128_f8f6f4 v[70:73], v[10:17], v[216:223], v[70:73]
	v_mfma_f32_16x16x128_f8f6f4 v[58:61], v[2:9], v[224:231], v[58:61]
	v_mfma_f32_16x16x128_f8f6f4 v[42:45], v[10:17], v[224:231], v[42:45]
	v_mfma_f32_16x16x128_f8f6f4 v[38:41], v[2:9], v[232:239], v[38:41]
	v_mfma_f32_16x16x128_f8f6f4 v[34:37], v[10:17], v[232:239], v[34:37]
	s_setprio 0
	s_setprio 1
	v_mfma_f32_16x16x128_f8f6f4 v[86:89], v[18:25], v[208:215], v[86:89]
	v_mfma_f32_16x16x128_f8f6f4 v[78:81], v[26:33], v[208:215], v[78:81]
	v_mfma_f32_16x16x128_f8f6f4 v[62:65], v[18:25], v[216:223], v[62:65]
	v_mfma_f32_16x16x128_f8f6f4 v[46:49], v[26:33], v[216:223], v[46:49]
	v_mfma_f32_16x16x128_f8f6f4 v[74:77], v[18:25], v[224:231], v[74:77]
	v_mfma_f32_16x16x128_f8f6f4 v[66:69], v[26:33], v[224:231], v[66:69]
	v_mfma_f32_16x16x128_f8f6f4 v[54:57], v[18:25], v[232:239], v[54:57]
	v_mfma_f32_16x16x128_f8f6f4 v[50:53], v[26:33], v[232:239], v[50:53]
	s_setprio 0
	s_add_i32 s91, s91, 2
	s_add_u32 s62, s62, 0x100
	s_addc_u32 s63, s63, 0
	s_add_u32 s41, s41, 0x100
	s_addc_u32 s90, s90, 0
	s_cmp_gt_u32 s91, 13
	s_barrier
	s_cbranch_scc0 .LBB0_831
	s_and_b64 vcc, exec, s[26:27]
	s_cbranch_vccz .LBB0_834
	s_barrier
